# speedup vs baseline: 1.0019x; 1.0019x over previous
.LBB1_5:
	s_waitcnt lgkmcnt(6)
	v_mfma_f32_32x32x64_f8f6f4 v[4:19], v[156:163], v[148:155], v[4:19]
	v_cmp_eq_u32_e32 vcc, 0, v1
	s_nop 1
	s_and_saveexec_b64 s[0:1], vcc
	s_lshl_b32 s12, s29, 2
	s_add_i32 s12, s12, 0x12000
	v_mov_b32_e32 v1, s12
	ds_write_b32 v1, v0
	s_or_b64 exec, exec, s[0:1]
	s_waitcnt vmcnt(0) lgkmcnt(0)
	s_barrier
	v_mov_b32_e32 v104, 0
	v_mov_b32_e32 v206, 0x12000
	ds_read_b128 v[38:41], v206
	ds_read_b128 v[42:45], v206 offset:16
	s_mov_b32 s14, 0
	v_mfma_f32_32x32x64_f8f6f4 v[20:35], v[164:171], v[148:155], v[20:35]
	v_mfma_f32_32x32x64_f8f6f4 v[4:19], v[80:87], v[72:79], v[4:19]
	v_mfma_f32_32x32x64_f8f6f4 v[20:35], v[58:65], v[72:79], v[20:35]
	s_waitcnt lgkmcnt(0)
	v_or_b32_e32 v0, v39, v38
	v_or_b32_e32 v0, v40, v0
	v_or_b32_e32 v0, v41, v0
	v_or_b32_e32 v0, v42, v0
	v_or_b32_e32 v0, v43, v0
	v_or_b32_e32 v0, v44, v0
	v_or_b32_e32 v0, v45, v0
	v_cmp_ne_u32_e32 vcc, 0, v0
	s_cbranch_vccnz .LBB1_13
	s_mov_b64 s[0:1], -1
	s_nop 8
	s_branch .Lfinal_copy

.LBB1_11:
	s_lshl_b32 s0, s30, 5
	s_lshl_b32 s1, s31, 7
	s_and_b32 s13, s2, 3
	s_or_b32 s14, s0, s1
	s_lshl_b32 s4, s28, 7
	s_lshl_b32 s5, s31, 2
	s_add_i32 s4, s4, s5
	s_add_i32 s4, s4, s30
	s_lshl_b32 s4, s4, 1
	s_add_i32 s4, s4, s3
	s_lshl_b32 s4, s4, 12
	s_add_u32 s4, s18, s4
	s_addc_u32 s5, s19, 0
	v_lshlrev_b32_e32 v0, 2, v173
	s_lshl_b32 s0, s3, 5
	s_lshl_b32 s12, s13, 6
	s_mov_b32 s1, 0
	s_mov_b32 s15, 0
	global_load_dwordx4 v[124:127], v0, s[4:5]
	global_load_dwordx4 v[128:131], v0, s[4:5] offset:1024
	global_load_dwordx4 v[132:135], v0, s[4:5] offset:2048
	global_load_dwordx4 v[136:139], v0, s[4:5] offset:3072
	s_lshl_b64 s[2:3], s[14:15], 2
	v_mov_b32_e32 v37, 0
	v_lshlrev_b32_e32 v36, 2, v172
	v_lshlrev_b32_e32 v122, 16, v175
	v_mov_b32_e32 v123, 0
	s_mul_i32 s4, s29, 0x2200
	s_add_i32 s4, s4, 0
	v_mov_b32_e32 v8, v141
	v_add_u32_e32 v9, s4, v173
	s_xor_b32 s4, s29, 4
	v_permlane32_swap_b32_e32 v141, v8
	s_mulk_i32 s4, 0x2200
	v_add_f32_e32 v8, v141, v8
	s_add_i32 s4, s4, 0
	ds_write2st64_b32 v9, v146, v8 offset1:1
	ds_write2st64_b32 v9, v86, v87 offset0:2 offset1:3
	ds_write2st64_b32 v9, v70, v71 offset0:18 offset1:19
	ds_write2st64_b32 v9, v88, v89 offset0:4 offset1:5
	ds_write2st64_b32 v9, v72, v73 offset0:20 offset1:21
	ds_write2st64_b32 v9, v90, v91 offset0:6 offset1:7
	ds_write2st64_b32 v9, v74, v75 offset0:22 offset1:23
	ds_write2st64_b32 v9, v92, v93 offset0:8 offset1:9
	ds_write2st64_b32 v9, v76, v77 offset0:24 offset1:25
	ds_write2st64_b32 v9, v94, v95 offset0:10 offset1:11
	ds_write2st64_b32 v9, v78, v79 offset0:26 offset1:27
	ds_write2st64_b32 v9, v96, v97 offset0:12 offset1:13
	ds_write2st64_b32 v9, v80, v81 offset0:28 offset1:29
	ds_write2st64_b32 v9, v98, v99 offset0:14 offset1:15
	ds_write2st64_b32 v9, v82, v83 offset0:30 offset1:31
	ds_write2st64_b32 v9, v100, v101 offset0:16 offset1:17
	ds_write2st64_b32 v9, v84, v85 offset0:32 offset1:33
	v_add_u32_e32 v66, s4, v173
	s_waitcnt lgkmcnt(0)
	s_barrier
	ds_read2st64_b32 v[10:11], v66 offset1:1
	ds_read2st64_b32 v[12:13], v66 offset0:2 offset1:3
	ds_read2st64_b32 v[14:15], v66 offset0:4 offset1:5
	ds_read2st64_b32 v[38:39], v66 offset0:6 offset1:7
	v_max_f32_e32 v40, v146, v146
	s_waitcnt lgkmcnt(3)
	v_max_f32_e32 v9, v10, v10
	v_max_f32_e32 v9, v40, v9
	v_sub_f32_e32 v40, v146, v9
	v_sub_f32_e32 v9, v10, v9
	v_exp_f32_e32 v40, v40
	v_exp_f32_e32 v41, v9
	v_mov_b32_e32 v9, v11
	v_pk_mul_f32 v[8:9], v[8:9], v[40:41]
	s_nop 0
	v_add_f32_e32 v8, v8, v9
	v_div_scale_f32 v9, s[4:5], v8, v8, 1.0
	v_rcp_f32_e32 v10, v9
	s_nop 0
	v_fma_f32 v11, -v9, v10, 1.0
	v_fmac_f32_e32 v10, v11, v10
	v_div_scale_f32 v11, vcc, 1.0, v8, 1.0
	v_mul_f32_e32 v42, v11, v10
	v_fma_f32 v43, -v9, v42, v11
	v_fmac_f32_e32 v42, v43, v10
	v_fma_f32 v9, -v9, v42, v11
	v_div_fmas_f32 v9, v9, v10, v42
	v_div_fixup_f32 v9, v9, v8, 1.0
	v_mul_f32_e32 v8, v40, v9
	v_mul_f32_e32 v10, v41, v9
	ds_read2st64_b32 v[40:41], v66 offset0:18 offset1:19
	ds_read2st64_b32 v[42:43], v66 offset0:20 offset1:21
	ds_read2st64_b32 v[44:45], v66 offset0:22 offset1:23
	ds_read2st64_b32 v[46:47], v66 offset0:16 offset1:17
	s_waitcnt lgkmcnt(6)
	v_pk_mul_f32 v[12:13], v[10:11], v[12:13] op_sel_hi:[0,1]
	s_waitcnt lgkmcnt(5)
	v_pk_mul_f32 v[14:15], v[10:11], v[14:15] op_sel_hi:[0,1]
	s_waitcnt lgkmcnt(4)
	v_pk_mul_f32 v[38:39], v[10:11], v[38:39] op_sel_hi:[0,1]
	s_waitcnt lgkmcnt(3)
	v_pk_mul_f32 v[40:41], v[10:11], v[40:41] op_sel_hi:[0,1]
	v_pk_fma_f32 v[48:49], v[8:9], v[70:71], v[40:41] op_sel_hi:[0,1,1]
	s_waitcnt lgkmcnt(2)
	v_pk_mul_f32 v[40:41], v[10:11], v[42:43] op_sel_hi:[0,1]
	v_pk_fma_f32 v[50:51], v[8:9], v[72:73], v[40:41] op_sel_hi:[0,1,1]
	s_waitcnt lgkmcnt(1)
	v_pk_mul_f32 v[40:41], v[10:11], v[44:45] op_sel_hi:[0,1]
	v_pk_fma_f32 v[52:53], v[8:9], v[74:75], v[40:41] op_sel_hi:[0,1,1]
	ds_read2st64_b32 v[40:41], v66 offset0:8 offset1:9
	ds_read2st64_b32 v[42:43], v66 offset0:24 offset1:25
	ds_read2st64_b32 v[44:45], v66 offset0:10 offset1:11
	ds_read2st64_b32 v[54:55], v66 offset0:12 offset1:13
	ds_read2st64_b32 v[56:57], v66 offset0:14 offset1:15
	ds_read2st64_b32 v[58:59], v66 offset0:26 offset1:27
	ds_read2st64_b32 v[60:61], v66 offset0:28 offset1:29
	ds_read2st64_b32 v[62:63], v66 offset0:30 offset1:31
	s_waitcnt lgkmcnt(6)
	v_pk_mul_f32 v[42:43], v[10:11], v[42:43] op_sel_hi:[0,1]
	v_pk_fma_f32 v[64:65], v[8:9], v[76:77], v[42:43] op_sel_hi:[0,1,1]
	s_waitcnt lgkmcnt(5)
	v_pk_mul_f32 v[42:43], v[10:11], v[44:45] op_sel_hi:[0,1]
	s_waitcnt lgkmcnt(2)
	v_pk_mul_f32 v[44:45], v[10:11], v[58:59] op_sel_hi:[0,1]
	v_pk_fma_f32 v[58:59], v[8:9], v[78:79], v[44:45] op_sel_hi:[0,1,1]
	v_pk_mul_f32 v[44:45], v[10:11], v[54:55] op_sel_hi:[0,1]
	s_waitcnt lgkmcnt(1)
	v_pk_mul_f32 v[54:55], v[10:11], v[60:61] op_sel_hi:[0,1]
	ds_read2st64_b32 v[60:61], v66 offset0:32 offset1:33
	s_waitcnt vmcnt(0)
	v_pk_mul_f32 v[40:41], v[10:11], v[40:41] op_sel_hi:[0,1]
	v_cvt_pk_bf16_f32 v0, v208, v209
	v_cvt_pk_bf16_f32 v1, v210, v211
	v_cvt_pk_bf16_f32 v2, v212, v213
	v_cvt_pk_bf16_f32 v3, v214, v215
	v_pk_fma_f32 v[12:13], v[8:9], v[86:87], v[12:13] op_sel_hi:[0,1,1]
	v_pk_fma_f32 v[14:15], v[8:9], v[88:89], v[14:15] op_sel_hi:[0,1,1]
	v_pk_fma_f32 v[38:39], v[8:9], v[90:91], v[38:39] op_sel_hi:[0,1,1]
	v_pk_fma_f32 v[40:41], v[8:9], v[92:93], v[40:41] op_sel_hi:[0,1,1]
	v_pk_mul_f32 v[56:57], v[10:11], v[56:57] op_sel_hi:[0,1]
	s_waitcnt lgkmcnt(1)
	v_pk_mul_f32 v[62:63], v[10:11], v[62:63] op_sel_hi:[0,1]
	v_pk_mul_f32 v[46:47], v[10:11], v[46:47] op_sel_hi:[0,1]
	s_waitcnt lgkmcnt(0)
	v_pk_mul_f32 v[10:11], v[10:11], v[60:61] op_sel_hi:[0,1]
	v_cvt_pk_bf16_f32 v4, v12, v13
	v_cvt_pk_bf16_f32 v5, v14, v15
	v_cvt_pk_bf16_f32 v6, v38, v39
	v_cvt_pk_bf16_f32 v7, v40, v41
	v_pk_fma_f32 v[42:43], v[8:9], v[94:95], v[42:43] op_sel_hi:[0,1,1]
	v_pk_fma_f32 v[44:45], v[8:9], v[96:97], v[44:45] op_sel_hi:[0,1,1]
	v_pk_fma_f32 v[54:55], v[8:9], v[80:81], v[54:55] op_sel_hi:[0,1,1]
	v_pk_fma_f32 v[56:57], v[8:9], v[98:99], v[56:57] op_sel_hi:[0,1,1]
	v_pk_fma_f32 v[62:63], v[8:9], v[82:83], v[62:63] op_sel_hi:[0,1,1]
	v_pk_fma_f32 v[46:47], v[8:9], v[100:101], v[46:47] op_sel_hi:[0,1,1]
	v_pk_fma_f32 v[60:61], v[8:9], v[84:85], v[10:11] op_sel_hi:[0,1,1]
	v_mfma_f32_32x32x16_bf16 v[0:15], v[0:3], v[4:7], 0
	v_cvt_pk_bf16_f32 v42, v42, v43
	v_cvt_pk_bf16_f32 v38, v216, v217
	v_cvt_pk_bf16_f32 v39, v218, v219
	v_cvt_pk_bf16_f32 v40, v220, v221
	v_cvt_pk_bf16_f32 v41, v222, v223
	v_cvt_pk_bf16_f32 v43, v44, v45
	v_cvt_pk_bf16_f32 v44, v56, v57
	v_cvt_pk_bf16_f32 v45, v46, v47
	s_nop 1
	v_mfma_f32_32x32x16_bf16 v[0:15], v[38:41], v[42:45], v[0:15]
	v_cvt_pk_bf16_f32 v38, v224, v225
	v_cvt_pk_bf16_f32 v39, v226, v227
	v_cvt_pk_bf16_f32 v40, v228, v229
	v_cvt_pk_bf16_f32 v41, v230, v231
	v_cvt_pk_bf16_f32 v42, v48, v49
	v_cvt_pk_bf16_f32 v43, v50, v51
	v_cvt_pk_bf16_f32 v44, v52, v53
	v_cvt_pk_bf16_f32 v45, v64, v65
	v_cvt_pk_bf16_f32 v32, v232, v233
	v_cvt_pk_bf16_f32 v33, v234, v235
	v_mfma_f32_32x32x16_bf16 v[0:15], v[38:41], v[42:45], v[0:15]
	v_cvt_pk_bf16_f32 v34, v236, v237
	v_cvt_pk_bf16_f32 v35, v238, v239
	v_cvt_pk_bf16_f32 v38, v58, v59
	v_add_f32_e32 v42, 1.0, v205
	v_div_scale_f32 v43, s[4:5], v42, v42, 1.0
	v_rcp_f32_e32 v44, v43
	v_cvt_pk_bf16_f32 v39, v54, v55
	v_cvt_pk_bf16_f32 v40, v62, v63
	v_cvt_pk_bf16_f32 v41, v60, v61
	s_lshl_b32 s4, s28, 8
	s_or_b32 s4, s4, s12
	v_mfma_f32_32x32x16_bf16 v[0:15], v[32:35], v[38:41], v[0:15]
	v_fma_f32 v32, -v43, v44, 1.0
	v_fmac_f32_e32 v44, v32, v44
	v_div_scale_f32 v32, vcc, 1.0, v42, 1.0
	s_add_i32 s0, s4, s0
	v_mul_f32_e32 v33, v32, v44
	s_lshl_b64 s[0:1], s[0:1], 14
	v_fma_f32 v34, -v43, v33, v32
	s_add_u32 s0, s10, s0
	v_fmac_f32_e32 v33, v34, v44
	s_addc_u32 s1, s11, s1
	v_fma_f32 v32, -v43, v33, v32
	s_add_u32 s0, s0, s2
	v_div_fmas_f32 v32, v32, v44, v33
	s_addc_u32 s1, s1, s3
	v_add_f32_e32 v0, v0, v240
	v_div_fixup_f32 v34, v32, v42, 1.0
	v_lshl_add_u64 v[32:33], s[0:1], 0, v[36:37]
	v_fmac_f32_e32 v124, v205, v0
	v_mul_f32_e32 v0, v34, v124
	v_lshl_add_u64 v[32:33], v[32:33], 0, v[122:123]
	global_store_dword v[32:33], v0, off sc1
	v_add_f32_e32 v0, v1, v241
	s_movk_i32 s0, 0x4000
	v_fmac_f32_e32 v125, v205, v0
	v_add_co_u32_e32 v0, vcc, s0, v32
	v_mul_f32_e32 v28, v34, v125
	s_nop 0
	v_addc_co_u32_e32 v1, vcc, 0, v33, vcc
	global_store_dword v[0:1], v28, off sc1
	v_add_f32_e32 v0, v2, v242
	s_mov_b32 s0, 0x8000
	v_fmac_f32_e32 v126, v205, v0
	v_add_co_u32_e32 v0, vcc, s0, v32
	v_mul_f32_e32 v2, v34, v126
	s_nop 0
	v_addc_co_u32_e32 v1, vcc, 0, v33, vcc
	global_store_dword v[0:1], v2, off sc1
	v_add_f32_e32 v0, v3, v243
	s_mov_b32 s0, 0xc000
	v_fmac_f32_e32 v127, v205, v0
	v_add_co_u32_e32 v0, vcc, s0, v32
	v_mul_f32_e32 v2, v34, v127
	s_nop 0
	v_addc_co_u32_e32 v1, vcc, 0, v33, vcc
	global_store_dword v[0:1], v2, off sc1
	v_add_f32_e32 v0, v4, v244
	s_mov_b32 s0, 0x20000
	v_fmac_f32_e32 v128, v205, v0
	v_add_co_u32_e32 v0, vcc, s0, v32
	v_mul_f32_e32 v2, v34, v128
	s_nop 0
	v_addc_co_u32_e32 v1, vcc, 0, v33, vcc
	global_store_dword v[0:1], v2, off sc1
	v_add_f32_e32 v0, v5, v245
	s_mov_b32 s0, 0x24000
	v_fmac_f32_e32 v129, v205, v0
	v_add_co_u32_e32 v0, vcc, s0, v32
	v_mul_f32_e32 v2, v34, v129
	s_nop 0
	v_addc_co_u32_e32 v1, vcc, 0, v33, vcc
	global_store_dword v[0:1], v2, off sc1
	v_add_f32_e32 v0, v6, v246
	s_mov_b32 s0, 0x28000
	v_fmac_f32_e32 v130, v205, v0
	v_add_co_u32_e32 v0, vcc, s0, v32
	v_mul_f32_e32 v2, v34, v130
	s_nop 0
	v_addc_co_u32_e32 v1, vcc, 0, v33, vcc
	global_store_dword v[0:1], v2, off sc1
	v_add_f32_e32 v0, v7, v247
	s_mov_b32 s0, 0x2c000
	v_fmac_f32_e32 v131, v205, v0
	v_add_co_u32_e32 v0, vcc, s0, v32
	v_mul_f32_e32 v2, v34, v131
	s_nop 0
	v_addc_co_u32_e32 v1, vcc, 0, v33, vcc
	global_store_dword v[0:1], v2, off sc1
	v_add_f32_e32 v0, v8, v248
	s_mov_b32 s0, 0x40000
	v_fmac_f32_e32 v132, v205, v0
	v_add_co_u32_e32 v0, vcc, s0, v32
	v_mul_f32_e32 v2, v34, v132
	s_nop 0
	v_addc_co_u32_e32 v1, vcc, 0, v33, vcc
	global_store_dword v[0:1], v2, off sc1
	v_add_f32_e32 v0, v9, v249
	s_mov_b32 s0, 0x44000
	v_fmac_f32_e32 v133, v205, v0
	v_add_co_u32_e32 v0, vcc, s0, v32
	v_mul_f32_e32 v2, v34, v133
	s_nop 0
	v_addc_co_u32_e32 v1, vcc, 0, v33, vcc
	global_store_dword v[0:1], v2, off sc1
	v_add_f32_e32 v0, v10, v250
	s_mov_b32 s0, 0x48000
	v_fmac_f32_e32 v134, v205, v0
	v_add_co_u32_e32 v0, vcc, s0, v32
	v_mul_f32_e32 v2, v34, v134
	s_nop 0
	v_addc_co_u32_e32 v1, vcc, 0, v33, vcc
	global_store_dword v[0:1], v2, off sc1
	v_add_f32_e32 v0, v11, v251
	s_mov_b32 s0, 0x4c000
	v_fmac_f32_e32 v135, v205, v0
	v_add_co_u32_e32 v0, vcc, s0, v32
	v_mul_f32_e32 v2, v34, v135
	s_nop 0
	v_addc_co_u32_e32 v1, vcc, 0, v33, vcc
	global_store_dword v[0:1], v2, off sc1
	v_add_f32_e32 v0, v12, v252
	s_mov_b32 s0, 0x60000
	v_fmac_f32_e32 v136, v205, v0
	v_add_co_u32_e32 v0, vcc, s0, v32
	v_mul_f32_e32 v2, v34, v136
	s_nop 0
	v_addc_co_u32_e32 v1, vcc, 0, v33, vcc
	global_store_dword v[0:1], v2, off sc1
	v_add_f32_e32 v0, v13, v253
	s_mov_b32 s0, 0x64000
	v_fmac_f32_e32 v137, v205, v0
	v_add_co_u32_e32 v0, vcc, s0, v32
	v_mul_f32_e32 v2, v34, v137
	s_nop 0
	v_addc_co_u32_e32 v1, vcc, 0, v33, vcc
	global_store_dword v[0:1], v2, off sc1
	v_add_f32_e32 v0, v14, v254
	s_mov_b32 s0, 0x68000
	v_fmac_f32_e32 v138, v205, v0
	v_add_co_u32_e32 v0, vcc, s0, v32
	v_mul_f32_e32 v2, v34, v138
	s_nop 0
	v_addc_co_u32_e32 v1, vcc, 0, v33, vcc
	global_store_dword v[0:1], v2, off sc1
	v_add_f32_e32 v0, v15, v255
	v_fmac_f32_e32 v139, v205, v0
	v_add_co_u32_e32 v0, vcc, 0x6c000, v32
	v_mul_f32_e32 v2, v34, v139
	s_nop 0
	v_addc_co_u32_e32 v1, vcc, 0, v33, vcc
	global_store_dword v[0:1], v2, off sc1
	s_endpgm
